# pipelined attention, weight-paced VALU, LDS staging writes and global loads spread over the whole tile
# baseline (speedup 1.0000x reference)
.LBB0_734:
	s_waitcnt lgkmcnt(0)
	s_barrier
	ds_read_b128 v[160:163], v201 offset:16384
	ds_read_b128 v[164:167], v209 offset:0
	ds_read_b128 v[168:171], v202 offset:16384
	ds_read_b128 v[172:175], v209 offset:2048
	ds_read_b128 v[176:179], v203 offset:16384
	ds_read_b128 v[180:183], v209 offset:4096
	ds_read_b128 v[230:233], v246 offset:16384
	s_waitcnt lgkmcnt(6)
	v_mfma_f32_16x16x32_bf16 v[64:67], v[160:163], v[96:99], 0
	v_exp_f32_e32 v88, v88
	v_mfma_f32_16x16x32_bf16 v[68:71], v[160:163], v[112:115], 0
	v_exp_f32_e32 v92, v92
	ds_read_b128 v[234:237], v209 offset:6144
	s_add_u32 s16, s22, s10
	s_addc_u32 s17, s23, s11
	s_add_u32 s15, s22, s12
	s_addc_u32 s14, s23, s13
	s_add_u32 s8, s16, 0x3bc00200
	s_addc_u32 s9, s17, 0
	s_add_u32 s6, s15, 0x23a50000
	s_addc_u32 s7, s14, 0
	s_waitcnt lgkmcnt(6)
	v_mfma_f32_16x16x32_bf16 v[0:3], v[164:167], v[216:219], v[0:3]
	v_cvt_pk_bf16_f32 v242, v80, v81
	v_mfma_f32_16x16x32_bf16 v[4:7], v[164:167], v[238:241], v[4:7]
	v_exp_f32_e32 v89, v89
	ds_read_b128 v[160:163], v201 offset:20480
	s_waitcnt vmcnt(4)
	ds_write_b128 v225, v[152:155] offset:49152
	s_waitcnt lgkmcnt(7)
	v_mfma_f32_16x16x32_bf16 v[68:71], v[168:171], v[116:119], v[68:71]
	v_exp_f32_e32 v93, v93
	v_mfma_f32_16x16x32_bf16 v[64:67], v[168:171], v[100:103], v[64:67]
	v_cvt_pk_bf16_f32 v243, v82, v83
	ds_read_b128 v[164:167], v209 offset:8192
	s_waitcnt lgkmcnt(7)
	v_mfma_f32_16x16x32_bf16 v[12:15], v[172:175], v[238:241], v[12:15]
	v_exp_f32_e32 v90, v90
	v_mfma_f32_16x16x32_bf16 v[8:11], v[172:175], v[216:219], v[8:11]
	v_exp_f32_e32 v94, v94
	ds_read_b128 v[168:171], v202 offset:20480
	s_waitcnt lgkmcnt(7)
	v_mfma_f32_16x16x32_bf16 v[64:67], v[176:179], v[104:107], v[64:67]
	v_cvt_pk_bf16_f32 v204, v84, v85
	v_mfma_f32_16x16x32_bf16 v[68:71], v[176:179], v[120:123], v[68:71]
	v_exp_f32_e32 v91, v91
	ds_read_b128 v[172:175], v209 offset:10240
	ds_write_b128 v226, v[156:159] offset:49152
	s_waitcnt lgkmcnt(8)
	v_mfma_f32_16x16x32_bf16 v[16:19], v[180:183], v[216:219], v[16:19]
	v_exp_f32_e32 v95, v95
	v_mfma_f32_16x16x32_bf16 v[20:23], v[180:183], v[238:241], v[20:23]
	v_cvt_pk_bf16_f32 v205, v86, v87
	v_add_f32_e32 v220, v220, v88
	ds_read_b128 v[176:179], v203 offset:20480
	s_waitcnt lgkmcnt(8)
	v_mfma_f32_16x16x32_bf16 v[68:71], v[230:233], v[124:127], v[68:71]
	v_add_f32_e32 v221, v221, v92
	v_add_f32_e32 v220, v220, v89
	v_mfma_f32_16x16x32_bf16 v[64:67], v[230:233], v[108:111], v[64:67]
	v_add_f32_e32 v221, v221, v93
	v_cvt_pk_bf16_f32 v244, v88, v89
	ds_read_b128 v[180:183], v209 offset:12288
	s_waitcnt lgkmcnt(8)
	v_mfma_f32_16x16x32_bf16 v[28:31], v[234:237], v[238:241], v[28:31]
	v_cvt_pk_bf16_f32 v245, v90, v91
	v_cvt_pk_bf16_f32 v206, v92, v93
	v_mfma_f32_16x16x32_bf16 v[24:27], v[234:237], v[216:219], v[24:27]
	v_cvt_pk_bf16_f32 v207, v94, v95
	ds_read_b128 v[230:233], v246 offset:20480
	ds_write_b64 v227, v[132:133] offset:32768
	s_waitcnt lgkmcnt(9)
	v_mfma_f32_16x16x32_bf16 v[72:75], v[160:163], v[96:99], 0
	v_add_f32_e32 v220, v220, v90
	v_add_f32_e32 v221, v221, v94
	v_mfma_f32_16x16x32_bf16 v[76:79], v[160:163], v[112:115], 0
	v_add_f32_e32 v220, v220, v91
	v_add_f32_e32 v221, v221, v95
	ds_read_b128 v[234:237], v209 offset:14336
	s_waitcnt lgkmcnt(8)
	v_mfma_f32_16x16x32_bf16 v[32:35], v[164:167], v[216:219], v[32:35]
	v_add_f32_e32 v194, v194, v220
	v_add_f32_e32 v195, v195, v221
	v_mfma_f32_16x16x32_bf16 v[36:39], v[164:167], v[238:241], v[36:39]
	v_exp_f32_e32 v64, v64
	ds_read_b128 v[160:163], v201 offset:24576
	s_waitcnt lgkmcnt(8)
	v_mfma_f32_16x16x32_bf16 v[76:79], v[168:171], v[116:119], v[76:79]
	v_exp_f32_e32 v68, v68
	v_mfma_f32_16x16x32_bf16 v[72:75], v[168:171], v[100:103], v[72:75]
	v_exp_f32_e32 v65, v65
	ds_read_b128 v[164:167], v210 offset:0
	ds_write_b64 v228, v[134:135] offset:32768
	s_waitcnt lgkmcnt(9)
	v_mfma_f32_16x16x32_bf16 v[44:47], v[172:175], v[238:241], v[44:47]
	v_exp_f32_e32 v69, v69
	v_mfma_f32_16x16x32_bf16 v[40:43], v[172:175], v[216:219], v[40:43]
	v_exp_f32_e32 v66, v66
	ds_read_b128 v[168:171], v202 offset:24576
	s_waitcnt lgkmcnt(8)
	v_mfma_f32_16x16x32_bf16 v[72:75], v[176:179], v[104:107], v[72:75]
	v_exp_f32_e32 v70, v70
	v_mfma_f32_16x16x32_bf16 v[76:79], v[176:179], v[120:123], v[76:79]
	v_exp_f32_e32 v67, v67
	ds_read_b128 v[172:175], v210 offset:2048
	s_waitcnt lgkmcnt(8)
	v_mfma_f32_16x16x32_bf16 v[48:51], v[180:183], v[216:219], v[48:51]
	v_exp_f32_e32 v71, v71
	v_mfma_f32_16x16x32_bf16 v[52:55], v[180:183], v[238:241], v[52:55]
	v_add_f32_e32 v220, v64, v65
	ds_read_b128 v[176:179], v203 offset:24576
	ds_write_b64 v229, v[128:129] offset:32768
	s_waitcnt lgkmcnt(9)
	v_mfma_f32_16x16x32_bf16 v[76:79], v[230:233], v[124:127], v[76:79]
	v_add_f32_e32 v221, v68, v69
	v_mfma_f32_16x16x32_bf16 v[72:75], v[230:233], v[108:111], v[72:75]
	v_add_f32_e32 v220, v220, v66
	ds_read_b128 v[180:183], v210 offset:4096
	s_waitcnt lgkmcnt(8)
	v_mfma_f32_16x16x32_bf16 v[60:63], v[234:237], v[238:241], v[60:63]
	v_add_f32_e32 v221, v221, v70
	v_add_f32_e32 v220, v220, v67
	v_mfma_f32_16x16x32_bf16 v[56:59], v[234:237], v[216:219], v[56:59]
	v_add_f32_e32 v221, v221, v71
	ds_read_b128 v[230:233], v246 offset:24576
	s_waitcnt lgkmcnt(8)
	v_mfma_f32_16x16x32_bf16 v[80:83], v[160:163], v[96:99], 0
	v_exp_f32_e32 v72, v72
	v_mfma_f32_16x16x32_bf16 v[84:87], v[160:163], v[112:115], 0
	v_exp_f32_e32 v76, v76
	ds_read_b128 v[234:237], v210 offset:6144
	ds_write_b64 v184, v[130:131] offset:32768
	s_waitcnt lgkmcnt(9)
	v_mfma_f32_16x16x32_bf16 v[0:3], v[164:167], v[242:245], v[0:3]
	v_exp_f32_e32 v73, v73
	v_mfma_f32_16x16x32_bf16 v[4:7], v[164:167], v[204:207], v[4:7]
	v_exp_f32_e32 v77, v77
	ds_read_b128 v[160:163], v201 offset:28672
	s_waitcnt lgkmcnt(8)
	v_mfma_f32_16x16x32_bf16 v[84:87], v[168:171], v[116:119], v[84:87]
	v_exp_f32_e32 v74, v74
	v_mfma_f32_16x16x32_bf16 v[80:83], v[168:171], v[100:103], v[80:83]
	v_exp_f32_e32 v78, v78
	ds_read_b128 v[164:167], v210 offset:8192
	s_waitcnt lgkmcnt(8)
	v_mfma_f32_16x16x32_bf16 v[12:15], v[172:175], v[204:207], v[12:15]
	v_exp_f32_e32 v75, v75
	v_mfma_f32_16x16x32_bf16 v[8:11], v[172:175], v[242:245], v[8:11]
	v_exp_f32_e32 v79, v79
	ds_read_b128 v[168:171], v202 offset:28672
	global_load_dwordx4 v[132:135], v198, s[8:9]
	s_waitcnt lgkmcnt(8)
	v_mfma_f32_16x16x32_bf16 v[80:83], v[176:179], v[104:107], v[80:83]
	v_add_f32_e32 v220, v220, v72
	v_add_f32_e32 v221, v221, v76
	v_mfma_f32_16x16x32_bf16 v[84:87], v[176:179], v[120:123], v[84:87]
	v_add_f32_e32 v220, v220, v73
	ds_read_b128 v[172:175], v210 offset:10240
	s_waitcnt lgkmcnt(7)
	v_mfma_f32_16x16x32_bf16 v[16:19], v[180:183], v[242:245], v[16:19]
	v_add_f32_e32 v221, v221, v77
	v_add_f32_e32 v220, v220, v74
	v_mfma_f32_16x16x32_bf16 v[20:23], v[180:183], v[204:207], v[20:23]
	v_add_f32_e32 v221, v221, v78
	ds_read_b128 v[176:179], v203 offset:28672
	s_waitcnt lgkmcnt(7)
	v_mfma_f32_16x16x32_bf16 v[84:87], v[230:233], v[124:127], v[84:87]
	v_add_f32_e32 v220, v220, v75
	v_add_f32_e32 v221, v221, v79
	v_mfma_f32_16x16x32_bf16 v[80:83], v[230:233], v[108:111], v[80:83]
	v_cvt_pk_bf16_f32 v216, v64, v65
	ds_read_b128 v[180:183], v210 offset:12288
	global_load_dwordx4 v[128:131], v199, s[8:9]
	s_waitcnt lgkmcnt(7)
	v_mfma_f32_16x16x32_bf16 v[28:31], v[234:237], v[204:207], v[28:31]
	v_cvt_pk_bf16_f32 v217, v66, v67
	v_cvt_pk_bf16_f32 v238, v68, v69
	v_mfma_f32_16x16x32_bf16 v[24:27], v[234:237], v[242:245], v[24:27]
	v_cvt_pk_bf16_f32 v239, v70, v71
	ds_read_b128 v[230:233], v246 offset:28672
	s_waitcnt lgkmcnt(6)
	v_mfma_f32_16x16x32_bf16 v[88:91], v[160:163], v[96:99], 0
	v_exp_f32_e32 v80, v80
	v_mfma_f32_16x16x32_bf16 v[92:95], v[160:163], v[112:115], 0
	v_exp_f32_e32 v84, v84
	ds_read_b128 v[234:237], v210 offset:14336
	s_waitcnt lgkmcnt(6)
	v_mfma_f32_16x16x32_bf16 v[32:35], v[164:167], v[242:245], v[32:35]
	v_exp_f32_e32 v81, v81
	v_mfma_f32_16x16x32_bf16 v[36:39], v[164:167], v[204:207], v[36:39]
	v_exp_f32_e32 v85, v85
	ds_read_b128 v[160:163], v201 offset:32768
	global_load_dwordx4 v[152:155], v196, s[6:7]
	s_waitcnt lgkmcnt(6)
	v_mfma_f32_16x16x32_bf16 v[92:95], v[168:171], v[116:119], v[92:95]
	v_exp_f32_e32 v82, v82
	v_mfma_f32_16x16x32_bf16 v[88:91], v[168:171], v[100:103], v[88:91]
	v_exp_f32_e32 v86, v86
	ds_read_b128 v[164:167], v209 offset:16384
	s_waitcnt lgkmcnt(6)
	v_mfma_f32_16x16x32_bf16 v[44:47], v[172:175], v[204:207], v[44:47]
	v_exp_f32_e32 v83, v83
	v_mfma_f32_16x16x32_bf16 v[40:43], v[172:175], v[242:245], v[40:43]
	v_exp_f32_e32 v87, v87
	ds_read_b128 v[168:171], v202 offset:32768
	s_waitcnt lgkmcnt(6)
	v_mfma_f32_16x16x32_bf16 v[88:91], v[176:179], v[104:107], v[88:91]
	v_add_f32_e32 v220, v220, v80
	v_add_f32_e32 v221, v221, v84
	v_mfma_f32_16x16x32_bf16 v[92:95], v[176:179], v[120:123], v[92:95]
	v_add_f32_e32 v220, v220, v81
	ds_read_b128 v[172:175], v209 offset:18432
	global_load_dwordx4 v[156:159], v197, s[6:7]
	s_waitcnt lgkmcnt(6)
	v_mfma_f32_16x16x32_bf16 v[48:51], v[180:183], v[242:245], v[48:51]
	v_add_f32_e32 v221, v221, v85
	v_add_f32_e32 v220, v220, v82
	v_mfma_f32_16x16x32_bf16 v[52:55], v[180:183], v[204:207], v[52:55]
	v_add_f32_e32 v221, v221, v86
	ds_read_b128 v[176:179], v203 offset:32768
	s_waitcnt lgkmcnt(6)
	v_mfma_f32_16x16x32_bf16 v[92:95], v[230:233], v[124:127], v[92:95]
	v_add_f32_e32 v220, v220, v83
	v_add_f32_e32 v221, v221, v87
	v_mfma_f32_16x16x32_bf16 v[88:91], v[230:233], v[108:111], v[88:91]
	v_cvt_pk_bf16_f32 v218, v72, v73
	ds_read_b128 v[180:183], v209 offset:20480
	s_waitcnt lgkmcnt(6)
	v_mfma_f32_16x16x32_bf16 v[60:63], v[234:237], v[204:207], v[60:63]
	v_cvt_pk_bf16_f32 v219, v74, v75
	v_cvt_pk_bf16_f32 v240, v76, v77
	v_mfma_f32_16x16x32_bf16 v[56:59], v[234:237], v[242:245], v[56:59]
	v_cvt_pk_bf16_f32 v241, v78, v79
	ds_read_b128 v[230:233], v246 offset:32768
	s_waitcnt lgkmcnt(6)
	v_mfma_f32_16x16x32_bf16 v[64:67], v[160:163], v[96:99], 0
	v_exp_f32_e32 v88, v88
	v_mfma_f32_16x16x32_bf16 v[68:71], v[160:163], v[112:115], 0
	v_exp_f32_e32 v92, v92
	ds_read_b128 v[234:237], v209 offset:22528
	s_add_u32 s8, s16, 0x3bc00280
	s_addc_u32 s9, s17, 0
	s_add_u32 s6, s15, 0x23a60000
	s_addc_u32 s7, s14, 0
	s_waitcnt lgkmcnt(6)
	v_mfma_f32_16x16x32_bf16 v[0:3], v[164:167], v[216:219], v[0:3]
	v_cvt_pk_bf16_f32 v242, v80, v81
	v_mfma_f32_16x16x32_bf16 v[4:7], v[164:167], v[238:241], v[4:7]
	v_exp_f32_e32 v89, v89
	ds_read_b128 v[160:163], v201 offset:36864
	s_waitcnt vmcnt(4)
	ds_write_b128 v225, v[136:139] offset:0
	s_waitcnt lgkmcnt(7)
	v_mfma_f32_16x16x32_bf16 v[68:71], v[168:171], v[116:119], v[68:71]
	v_exp_f32_e32 v93, v93
	v_mfma_f32_16x16x32_bf16 v[64:67], v[168:171], v[100:103], v[64:67]
	v_cvt_pk_bf16_f32 v243, v82, v83
	ds_read_b128 v[164:167], v209 offset:24576
	s_waitcnt lgkmcnt(7)
	v_mfma_f32_16x16x32_bf16 v[12:15], v[172:175], v[238:241], v[12:15]
	v_exp_f32_e32 v90, v90
	v_mfma_f32_16x16x32_bf16 v[8:11], v[172:175], v[216:219], v[8:11]
	v_exp_f32_e32 v94, v94
	ds_read_b128 v[168:171], v202 offset:36864
	s_waitcnt lgkmcnt(7)
	v_mfma_f32_16x16x32_bf16 v[64:67], v[176:179], v[104:107], v[64:67]
	v_cvt_pk_bf16_f32 v204, v84, v85
	v_mfma_f32_16x16x32_bf16 v[68:71], v[176:179], v[120:123], v[68:71]
	v_exp_f32_e32 v91, v91
	ds_read_b128 v[172:175], v209 offset:26624
	ds_write_b128 v226, v[140:143] offset:0
	s_waitcnt lgkmcnt(8)
	v_mfma_f32_16x16x32_bf16 v[16:19], v[180:183], v[216:219], v[16:19]
	v_exp_f32_e32 v95, v95
	v_mfma_f32_16x16x32_bf16 v[20:23], v[180:183], v[238:241], v[20:23]
	v_cvt_pk_bf16_f32 v205, v86, v87
	v_add_f32_e32 v220, v220, v88
	ds_read_b128 v[176:179], v203 offset:36864
	s_waitcnt lgkmcnt(8)
	v_mfma_f32_16x16x32_bf16 v[68:71], v[230:233], v[124:127], v[68:71]
	v_add_f32_e32 v221, v221, v92
	v_add_f32_e32 v220, v220, v89
	v_mfma_f32_16x16x32_bf16 v[64:67], v[230:233], v[108:111], v[64:67]
	v_add_f32_e32 v221, v221, v93
	v_cvt_pk_bf16_f32 v244, v88, v89
	ds_read_b128 v[180:183], v209 offset:28672
	s_waitcnt lgkmcnt(8)
	v_mfma_f32_16x16x32_bf16 v[28:31], v[234:237], v[238:241], v[28:31]
	v_cvt_pk_bf16_f32 v245, v90, v91
	v_cvt_pk_bf16_f32 v206, v92, v93
	v_mfma_f32_16x16x32_bf16 v[24:27], v[234:237], v[216:219], v[24:27]
	v_cvt_pk_bf16_f32 v207, v94, v95
	ds_read_b128 v[230:233], v246 offset:36864
	ds_write_b64 v227, v[148:149] offset:49152
	s_waitcnt lgkmcnt(9)
	v_mfma_f32_16x16x32_bf16 v[72:75], v[160:163], v[96:99], 0
	v_add_f32_e32 v220, v220, v90
	v_add_f32_e32 v221, v221, v94
	v_mfma_f32_16x16x32_bf16 v[76:79], v[160:163], v[112:115], 0
	v_add_f32_e32 v220, v220, v91
	v_add_f32_e32 v221, v221, v95
	ds_read_b128 v[234:237], v209 offset:30720
	s_waitcnt lgkmcnt(8)
	v_mfma_f32_16x16x32_bf16 v[32:35], v[164:167], v[216:219], v[32:35]
	v_add_f32_e32 v194, v194, v220
	v_add_f32_e32 v195, v195, v221
	v_mfma_f32_16x16x32_bf16 v[36:39], v[164:167], v[238:241], v[36:39]
	v_exp_f32_e32 v64, v64
	ds_read_b128 v[160:163], v201 offset:40960
	s_waitcnt lgkmcnt(8)
	v_mfma_f32_16x16x32_bf16 v[76:79], v[168:171], v[116:119], v[76:79]
	v_exp_f32_e32 v68, v68
	v_mfma_f32_16x16x32_bf16 v[72:75], v[168:171], v[100:103], v[72:75]
	v_exp_f32_e32 v65, v65
	ds_read_b128 v[164:167], v210 offset:16384
	ds_write_b64 v228, v[150:151] offset:49152
	s_waitcnt lgkmcnt(9)
	v_mfma_f32_16x16x32_bf16 v[44:47], v[172:175], v[238:241], v[44:47]
	v_exp_f32_e32 v69, v69
	v_mfma_f32_16x16x32_bf16 v[40:43], v[172:175], v[216:219], v[40:43]
	v_exp_f32_e32 v66, v66
	ds_read_b128 v[168:171], v202 offset:40960
	s_waitcnt lgkmcnt(8)
	v_mfma_f32_16x16x32_bf16 v[72:75], v[176:179], v[104:107], v[72:75]
	v_exp_f32_e32 v70, v70
	v_mfma_f32_16x16x32_bf16 v[76:79], v[176:179], v[120:123], v[76:79]
	v_exp_f32_e32 v67, v67
	ds_read_b128 v[172:175], v210 offset:18432
	s_waitcnt lgkmcnt(8)
	v_mfma_f32_16x16x32_bf16 v[48:51], v[180:183], v[216:219], v[48:51]
	v_exp_f32_e32 v71, v71
	v_mfma_f32_16x16x32_bf16 v[52:55], v[180:183], v[238:241], v[52:55]
	v_add_f32_e32 v220, v64, v65
	ds_read_b128 v[176:179], v203 offset:40960
	ds_write_b64 v229, v[144:145] offset:49152
	s_waitcnt lgkmcnt(9)
	v_mfma_f32_16x16x32_bf16 v[76:79], v[230:233], v[124:127], v[76:79]
	v_add_f32_e32 v221, v68, v69
	v_mfma_f32_16x16x32_bf16 v[72:75], v[230:233], v[108:111], v[72:75]
	v_add_f32_e32 v220, v220, v66
	ds_read_b128 v[180:183], v210 offset:20480
	s_waitcnt lgkmcnt(8)
	v_mfma_f32_16x16x32_bf16 v[60:63], v[234:237], v[238:241], v[60:63]
	v_add_f32_e32 v221, v221, v70
	v_add_f32_e32 v220, v220, v67
	v_mfma_f32_16x16x32_bf16 v[56:59], v[234:237], v[216:219], v[56:59]
	v_add_f32_e32 v221, v221, v71
	ds_read_b128 v[230:233], v246 offset:40960
	s_waitcnt lgkmcnt(8)
	v_mfma_f32_16x16x32_bf16 v[80:83], v[160:163], v[96:99], 0
	v_exp_f32_e32 v72, v72
	v_mfma_f32_16x16x32_bf16 v[84:87], v[160:163], v[112:115], 0
	v_exp_f32_e32 v76, v76
	ds_read_b128 v[234:237], v210 offset:22528
	ds_write_b64 v184, v[146:147] offset:49152
	s_waitcnt lgkmcnt(9)
	v_mfma_f32_16x16x32_bf16 v[0:3], v[164:167], v[242:245], v[0:3]
	v_exp_f32_e32 v73, v73
	v_mfma_f32_16x16x32_bf16 v[4:7], v[164:167], v[204:207], v[4:7]
	v_exp_f32_e32 v77, v77
	ds_read_b128 v[160:163], v201 offset:45056
	s_waitcnt lgkmcnt(8)
	v_mfma_f32_16x16x32_bf16 v[84:87], v[168:171], v[116:119], v[84:87]
	v_exp_f32_e32 v74, v74
	v_mfma_f32_16x16x32_bf16 v[80:83], v[168:171], v[100:103], v[80:83]
	v_exp_f32_e32 v78, v78
	ds_read_b128 v[164:167], v210 offset:24576
	s_waitcnt lgkmcnt(8)
	v_mfma_f32_16x16x32_bf16 v[12:15], v[172:175], v[204:207], v[12:15]
	v_exp_f32_e32 v75, v75
	v_mfma_f32_16x16x32_bf16 v[8:11], v[172:175], v[242:245], v[8:11]
	v_exp_f32_e32 v79, v79
	ds_read_b128 v[168:171], v202 offset:45056
	global_load_dwordx4 v[148:151], v198, s[8:9]
	s_waitcnt lgkmcnt(8)
	v_mfma_f32_16x16x32_bf16 v[80:83], v[176:179], v[104:107], v[80:83]
	v_add_f32_e32 v220, v220, v72
	v_add_f32_e32 v221, v221, v76
	v_mfma_f32_16x16x32_bf16 v[84:87], v[176:179], v[120:123], v[84:87]
	v_add_f32_e32 v220, v220, v73
	ds_read_b128 v[172:175], v210 offset:26624
	s_waitcnt lgkmcnt(7)
	v_mfma_f32_16x16x32_bf16 v[16:19], v[180:183], v[242:245], v[16:19]
	v_add_f32_e32 v221, v221, v77
	v_add_f32_e32 v220, v220, v74
	v_mfma_f32_16x16x32_bf16 v[20:23], v[180:183], v[204:207], v[20:23]
	v_add_f32_e32 v221, v221, v78
	ds_read_b128 v[176:179], v203 offset:45056
	s_waitcnt lgkmcnt(7)
	v_mfma_f32_16x16x32_bf16 v[84:87], v[230:233], v[124:127], v[84:87]
	v_add_f32_e32 v220, v220, v75
	v_add_f32_e32 v221, v221, v79
	v_mfma_f32_16x16x32_bf16 v[80:83], v[230:233], v[108:111], v[80:83]
	v_cvt_pk_bf16_f32 v216, v64, v65
	ds_read_b128 v[180:183], v210 offset:28672
	global_load_dwordx4 v[144:147], v199, s[8:9]
	s_waitcnt lgkmcnt(7)
	v_mfma_f32_16x16x32_bf16 v[28:31], v[234:237], v[204:207], v[28:31]
	v_cvt_pk_bf16_f32 v217, v66, v67
	v_cvt_pk_bf16_f32 v238, v68, v69
	v_mfma_f32_16x16x32_bf16 v[24:27], v[234:237], v[242:245], v[24:27]
	v_cvt_pk_bf16_f32 v239, v70, v71
	ds_read_b128 v[230:233], v246 offset:45056
	s_waitcnt lgkmcnt(6)
	v_mfma_f32_16x16x32_bf16 v[88:91], v[160:163], v[96:99], 0
	v_exp_f32_e32 v80, v80
	v_mfma_f32_16x16x32_bf16 v[92:95], v[160:163], v[112:115], 0
	v_exp_f32_e32 v84, v84
	ds_read_b128 v[234:237], v210 offset:30720
	s_waitcnt lgkmcnt(6)
	v_mfma_f32_16x16x32_bf16 v[32:35], v[164:167], v[242:245], v[32:35]
	v_exp_f32_e32 v81, v81
	v_mfma_f32_16x16x32_bf16 v[36:39], v[164:167], v[204:207], v[36:39]
	v_exp_f32_e32 v85, v85
	global_load_dwordx4 v[136:139], v196, s[6:7]
	s_waitcnt lgkmcnt(5)
	v_mfma_f32_16x16x32_bf16 v[92:95], v[168:171], v[116:119], v[92:95]
	v_exp_f32_e32 v82, v82
	v_mfma_f32_16x16x32_bf16 v[88:91], v[168:171], v[100:103], v[88:91]
	v_exp_f32_e32 v86, v86
	s_waitcnt lgkmcnt(4)
	v_mfma_f32_16x16x32_bf16 v[44:47], v[172:175], v[204:207], v[44:47]
	v_exp_f32_e32 v83, v83
	v_mfma_f32_16x16x32_bf16 v[40:43], v[172:175], v[242:245], v[40:43]
	v_exp_f32_e32 v87, v87
	s_waitcnt lgkmcnt(3)
	v_mfma_f32_16x16x32_bf16 v[88:91], v[176:179], v[104:107], v[88:91]
	v_add_f32_e32 v220, v220, v80
	v_add_f32_e32 v221, v221, v84
	v_mfma_f32_16x16x32_bf16 v[92:95], v[176:179], v[120:123], v[92:95]
	v_add_f32_e32 v220, v220, v81
	global_load_dwordx4 v[140:143], v197, s[6:7]
	s_waitcnt lgkmcnt(2)
	v_mfma_f32_16x16x32_bf16 v[48:51], v[180:183], v[242:245], v[48:51]
	v_add_f32_e32 v221, v221, v85
	v_add_f32_e32 v220, v220, v82
	v_mfma_f32_16x16x32_bf16 v[52:55], v[180:183], v[204:207], v[52:55]
	v_add_f32_e32 v221, v221, v86
	s_waitcnt lgkmcnt(1)
	v_mfma_f32_16x16x32_bf16 v[92:95], v[230:233], v[124:127], v[92:95]
	v_add_f32_e32 v220, v220, v83
	v_add_f32_e32 v221, v221, v87
	v_mfma_f32_16x16x32_bf16 v[88:91], v[230:233], v[108:111], v[88:91]
	v_cvt_pk_bf16_f32 v218, v72, v73
	s_waitcnt lgkmcnt(0)
	v_mfma_f32_16x16x32_bf16 v[60:63], v[234:237], v[204:207], v[60:63]
	v_cvt_pk_bf16_f32 v219, v74, v75
	v_cvt_pk_bf16_f32 v240, v76, v77
	v_mfma_f32_16x16x32_bf16 v[56:59], v[234:237], v[242:245], v[56:59]
	v_cvt_pk_bf16_f32 v241, v78, v79
	s_waitcnt lgkmcnt(0)
	s_barrier
	ds_read_b128 v[160:163], v201 offset:49152
	ds_read_b128 v[164:167], v209 offset:32768
	ds_read_b128 v[168:171], v202 offset:49152
	ds_read_b128 v[172:175], v209 offset:34816
	ds_read_b128 v[176:179], v203 offset:49152
	ds_read_b128 v[180:183], v209 offset:36864
	ds_read_b128 v[230:233], v246 offset:49152
	s_waitcnt lgkmcnt(6)
	v_mfma_f32_16x16x32_bf16 v[64:67], v[160:163], v[96:99], 0
	v_exp_f32_e32 v88, v88
	v_mfma_f32_16x16x32_bf16 v[68:71], v[160:163], v[112:115], 0
	v_exp_f32_e32 v92, v92
	ds_read_b128 v[234:237], v209 offset:38912
	s_add_u32 s8, s16, 0x3bc00300
	s_addc_u32 s9, s17, 0
	s_add_u32 s6, s15, 0x23a70000
	s_addc_u32 s7, s14, 0
	s_waitcnt lgkmcnt(6)
	v_mfma_f32_16x16x32_bf16 v[0:3], v[164:167], v[216:219], v[0:3]
	v_cvt_pk_bf16_f32 v242, v80, v81
	v_mfma_f32_16x16x32_bf16 v[4:7], v[164:167], v[238:241], v[4:7]
	v_exp_f32_e32 v89, v89
	ds_read_b128 v[160:163], v201 offset:53248
	s_waitcnt vmcnt(4)
	ds_write_b128 v225, v[152:155] offset:16384
	s_waitcnt lgkmcnt(7)
	v_mfma_f32_16x16x32_bf16 v[68:71], v[168:171], v[116:119], v[68:71]
	v_exp_f32_e32 v93, v93
	v_mfma_f32_16x16x32_bf16 v[64:67], v[168:171], v[100:103], v[64:67]
	v_cvt_pk_bf16_f32 v243, v82, v83
	ds_read_b128 v[164:167], v209 offset:40960
	s_waitcnt lgkmcnt(7)
	v_mfma_f32_16x16x32_bf16 v[12:15], v[172:175], v[238:241], v[12:15]
	v_exp_f32_e32 v90, v90
	v_mfma_f32_16x16x32_bf16 v[8:11], v[172:175], v[216:219], v[8:11]
	v_exp_f32_e32 v94, v94
	ds_read_b128 v[168:171], v202 offset:53248
	s_waitcnt lgkmcnt(7)
	v_mfma_f32_16x16x32_bf16 v[64:67], v[176:179], v[104:107], v[64:67]
	v_cvt_pk_bf16_f32 v204, v84, v85
	v_mfma_f32_16x16x32_bf16 v[68:71], v[176:179], v[120:123], v[68:71]
	v_exp_f32_e32 v91, v91
	ds_read_b128 v[172:175], v209 offset:43008
	ds_write_b128 v226, v[156:159] offset:16384
	s_waitcnt lgkmcnt(8)
	v_mfma_f32_16x16x32_bf16 v[16:19], v[180:183], v[216:219], v[16:19]
	v_exp_f32_e32 v95, v95
	v_mfma_f32_16x16x32_bf16 v[20:23], v[180:183], v[238:241], v[20:23]
	v_cvt_pk_bf16_f32 v205, v86, v87
	v_add_f32_e32 v220, v220, v88
	ds_read_b128 v[176:179], v203 offset:53248
	s_waitcnt lgkmcnt(8)
	v_mfma_f32_16x16x32_bf16 v[68:71], v[230:233], v[124:127], v[68:71]
	v_add_f32_e32 v221, v221, v92
	v_add_f32_e32 v220, v220, v89
	v_mfma_f32_16x16x32_bf16 v[64:67], v[230:233], v[108:111], v[64:67]
	v_add_f32_e32 v221, v221, v93
	v_cvt_pk_bf16_f32 v244, v88, v89
	ds_read_b128 v[180:183], v209 offset:45056
	s_waitcnt lgkmcnt(8)
	v_mfma_f32_16x16x32_bf16 v[28:31], v[234:237], v[238:241], v[28:31]
	v_cvt_pk_bf16_f32 v245, v90, v91
	v_cvt_pk_bf16_f32 v206, v92, v93
	v_mfma_f32_16x16x32_bf16 v[24:27], v[234:237], v[216:219], v[24:27]
	v_cvt_pk_bf16_f32 v207, v94, v95
	ds_read_b128 v[230:233], v246 offset:53248
	ds_write_b64 v227, v[132:133] offset:0
	s_waitcnt lgkmcnt(9)
	v_mfma_f32_16x16x32_bf16 v[72:75], v[160:163], v[96:99], 0
	v_add_f32_e32 v220, v220, v90
	v_add_f32_e32 v221, v221, v94
	v_mfma_f32_16x16x32_bf16 v[76:79], v[160:163], v[112:115], 0
	v_add_f32_e32 v220, v220, v91
	v_add_f32_e32 v221, v221, v95
	ds_read_b128 v[234:237], v209 offset:47104
	s_waitcnt lgkmcnt(8)
	v_mfma_f32_16x16x32_bf16 v[32:35], v[164:167], v[216:219], v[32:35]
	v_add_f32_e32 v194, v194, v220
	v_add_f32_e32 v195, v195, v221
	v_mfma_f32_16x16x32_bf16 v[36:39], v[164:167], v[238:241], v[36:39]
	v_exp_f32_e32 v64, v64
	ds_read_b128 v[160:163], v201 offset:57344
	s_waitcnt lgkmcnt(8)
	v_mfma_f32_16x16x32_bf16 v[76:79], v[168:171], v[116:119], v[76:79]
	v_exp_f32_e32 v68, v68
	v_mfma_f32_16x16x32_bf16 v[72:75], v[168:171], v[100:103], v[72:75]
	v_exp_f32_e32 v65, v65
	ds_read_b128 v[164:167], v210 offset:32768
	ds_write_b64 v228, v[134:135] offset:0
	s_waitcnt lgkmcnt(9)
	v_mfma_f32_16x16x32_bf16 v[44:47], v[172:175], v[238:241], v[44:47]
	v_exp_f32_e32 v69, v69
	v_mfma_f32_16x16x32_bf16 v[40:43], v[172:175], v[216:219], v[40:43]
	v_exp_f32_e32 v66, v66
	ds_read_b128 v[168:171], v202 offset:57344
	s_waitcnt lgkmcnt(8)
	v_mfma_f32_16x16x32_bf16 v[72:75], v[176:179], v[104:107], v[72:75]
	v_exp_f32_e32 v70, v70
	v_mfma_f32_16x16x32_bf16 v[76:79], v[176:179], v[120:123], v[76:79]
	v_exp_f32_e32 v67, v67
	ds_read_b128 v[172:175], v210 offset:34816
	s_waitcnt lgkmcnt(8)
	v_mfma_f32_16x16x32_bf16 v[48:51], v[180:183], v[216:219], v[48:51]
	v_exp_f32_e32 v71, v71
	v_mfma_f32_16x16x32_bf16 v[52:55], v[180:183], v[238:241], v[52:55]
	v_add_f32_e32 v220, v64, v65
	ds_read_b128 v[176:179], v203 offset:57344
	ds_write_b64 v229, v[128:129] offset:0
	s_waitcnt lgkmcnt(9)
	v_mfma_f32_16x16x32_bf16 v[76:79], v[230:233], v[124:127], v[76:79]
	v_add_f32_e32 v221, v68, v69
	v_mfma_f32_16x16x32_bf16 v[72:75], v[230:233], v[108:111], v[72:75]
	v_add_f32_e32 v220, v220, v66
	ds_read_b128 v[180:183], v210 offset:36864
	s_waitcnt lgkmcnt(8)
	v_mfma_f32_16x16x32_bf16 v[60:63], v[234:237], v[238:241], v[60:63]
	v_add_f32_e32 v221, v221, v70
	v_add_f32_e32 v220, v220, v67
	v_mfma_f32_16x16x32_bf16 v[56:59], v[234:237], v[216:219], v[56:59]
	v_add_f32_e32 v221, v221, v71
	ds_read_b128 v[230:233], v246 offset:57344
	s_waitcnt lgkmcnt(8)
	v_mfma_f32_16x16x32_bf16 v[80:83], v[160:163], v[96:99], 0
	v_exp_f32_e32 v72, v72
	v_mfma_f32_16x16x32_bf16 v[84:87], v[160:163], v[112:115], 0
	v_exp_f32_e32 v76, v76
	ds_read_b128 v[234:237], v210 offset:38912
	ds_write_b64 v184, v[130:131] offset:0
	s_waitcnt lgkmcnt(9)
	v_mfma_f32_16x16x32_bf16 v[0:3], v[164:167], v[242:245], v[0:3]
	v_exp_f32_e32 v73, v73
	v_mfma_f32_16x16x32_bf16 v[4:7], v[164:167], v[204:207], v[4:7]
	v_exp_f32_e32 v77, v77
	ds_read_b128 v[160:163], v201 offset:61440
	s_waitcnt lgkmcnt(8)
	v_mfma_f32_16x16x32_bf16 v[84:87], v[168:171], v[116:119], v[84:87]
	v_exp_f32_e32 v74, v74
	v_mfma_f32_16x16x32_bf16 v[80:83], v[168:171], v[100:103], v[80:83]
	v_exp_f32_e32 v78, v78
	ds_read_b128 v[164:167], v210 offset:40960
	s_waitcnt lgkmcnt(8)
	v_mfma_f32_16x16x32_bf16 v[12:15], v[172:175], v[204:207], v[12:15]
	v_exp_f32_e32 v75, v75
	v_mfma_f32_16x16x32_bf16 v[8:11], v[172:175], v[242:245], v[8:11]
	v_exp_f32_e32 v79, v79
	ds_read_b128 v[168:171], v202 offset:61440
	global_load_dwordx4 v[132:135], v198, s[8:9]
	s_waitcnt lgkmcnt(8)
	v_mfma_f32_16x16x32_bf16 v[80:83], v[176:179], v[104:107], v[80:83]
	v_add_f32_e32 v220, v220, v72
	v_add_f32_e32 v221, v221, v76
	v_mfma_f32_16x16x32_bf16 v[84:87], v[176:179], v[120:123], v[84:87]
	v_add_f32_e32 v220, v220, v73
	ds_read_b128 v[172:175], v210 offset:43008
	s_waitcnt lgkmcnt(7)
	v_mfma_f32_16x16x32_bf16 v[16:19], v[180:183], v[242:245], v[16:19]
	v_add_f32_e32 v221, v221, v77
	v_add_f32_e32 v220, v220, v74
	v_mfma_f32_16x16x32_bf16 v[20:23], v[180:183], v[204:207], v[20:23]
	v_add_f32_e32 v221, v221, v78
	ds_read_b128 v[176:179], v203 offset:61440
	s_waitcnt lgkmcnt(7)
	v_mfma_f32_16x16x32_bf16 v[84:87], v[230:233], v[124:127], v[84:87]
	v_add_f32_e32 v220, v220, v75
	v_add_f32_e32 v221, v221, v79
	v_mfma_f32_16x16x32_bf16 v[80:83], v[230:233], v[108:111], v[80:83]
	v_cvt_pk_bf16_f32 v216, v64, v65
	ds_read_b128 v[180:183], v210 offset:45056
	global_load_dwordx4 v[128:131], v199, s[8:9]
	s_waitcnt lgkmcnt(7)
	v_mfma_f32_16x16x32_bf16 v[28:31], v[234:237], v[204:207], v[28:31]
	v_cvt_pk_bf16_f32 v217, v66, v67
	v_cvt_pk_bf16_f32 v238, v68, v69
	v_mfma_f32_16x16x32_bf16 v[24:27], v[234:237], v[242:245], v[24:27]
	v_cvt_pk_bf16_f32 v239, v70, v71
	ds_read_b128 v[230:233], v246 offset:61440
	s_waitcnt lgkmcnt(6)
	v_mfma_f32_16x16x32_bf16 v[88:91], v[160:163], v[96:99], 0
	v_exp_f32_e32 v80, v80
	v_mfma_f32_16x16x32_bf16 v[92:95], v[160:163], v[112:115], 0
	v_exp_f32_e32 v84, v84
	ds_read_b128 v[234:237], v210 offset:47104
	s_waitcnt lgkmcnt(6)
	v_mfma_f32_16x16x32_bf16 v[32:35], v[164:167], v[242:245], v[32:35]
	v_exp_f32_e32 v81, v81
	v_mfma_f32_16x16x32_bf16 v[36:39], v[164:167], v[204:207], v[36:39]
	v_exp_f32_e32 v85, v85
	ds_read_b128 v[160:163], v201 offset:0
	global_load_dwordx4 v[152:155], v196, s[6:7]
	s_waitcnt lgkmcnt(6)
	v_mfma_f32_16x16x32_bf16 v[92:95], v[168:171], v[116:119], v[92:95]
	v_exp_f32_e32 v82, v82
	v_mfma_f32_16x16x32_bf16 v[88:91], v[168:171], v[100:103], v[88:91]
	v_exp_f32_e32 v86, v86
	ds_read_b128 v[164:167], v209 offset:49152
	s_waitcnt lgkmcnt(6)
	v_mfma_f32_16x16x32_bf16 v[44:47], v[172:175], v[204:207], v[44:47]
	v_exp_f32_e32 v83, v83
	v_mfma_f32_16x16x32_bf16 v[40:43], v[172:175], v[242:245], v[40:43]
	v_exp_f32_e32 v87, v87
	ds_read_b128 v[168:171], v202 offset:0
	s_waitcnt lgkmcnt(6)
	v_mfma_f32_16x16x32_bf16 v[88:91], v[176:179], v[104:107], v[88:91]
	v_add_f32_e32 v220, v220, v80
	v_add_f32_e32 v221, v221, v84
	v_mfma_f32_16x16x32_bf16 v[92:95], v[176:179], v[120:123], v[92:95]
	v_add_f32_e32 v220, v220, v81
	ds_read_b128 v[172:175], v209 offset:51200
	global_load_dwordx4 v[156:159], v197, s[6:7]
	s_waitcnt lgkmcnt(6)
	v_mfma_f32_16x16x32_bf16 v[48:51], v[180:183], v[242:245], v[48:51]
	v_add_f32_e32 v221, v221, v85
	v_add_f32_e32 v220, v220, v82
	v_mfma_f32_16x16x32_bf16 v[52:55], v[180:183], v[204:207], v[52:55]
	v_add_f32_e32 v221, v221, v86
	ds_read_b128 v[176:179], v203 offset:0
	s_waitcnt lgkmcnt(6)
	v_mfma_f32_16x16x32_bf16 v[92:95], v[230:233], v[124:127], v[92:95]
	v_add_f32_e32 v220, v220, v83
	v_add_f32_e32 v221, v221, v87
	v_mfma_f32_16x16x32_bf16 v[88:91], v[230:233], v[108:111], v[88:91]
	v_cvt_pk_bf16_f32 v218, v72, v73
	ds_read_b128 v[180:183], v209 offset:53248
	s_waitcnt lgkmcnt(6)
	v_mfma_f32_16x16x32_bf16 v[60:63], v[234:237], v[204:207], v[60:63]
	v_cvt_pk_bf16_f32 v219, v74, v75
	v_cvt_pk_bf16_f32 v240, v76, v77
	v_mfma_f32_16x16x32_bf16 v[56:59], v[234:237], v[242:245], v[56:59]
	v_cvt_pk_bf16_f32 v241, v78, v79
	ds_read_b128 v[230:233], v246 offset:0
	s_waitcnt lgkmcnt(6)
	v_mfma_f32_16x16x32_bf16 v[64:67], v[160:163], v[96:99], 0
	v_exp_f32_e32 v88, v88
	v_mfma_f32_16x16x32_bf16 v[68:71], v[160:163], v[112:115], 0
	v_exp_f32_e32 v92, v92
	ds_read_b128 v[234:237], v209 offset:55296
	s_add_u32 s8, s16, 0x3bc00380
	s_addc_u32 s9, s17, 0
	s_add_u32 s6, s15, 0x23a80000
	s_addc_u32 s7, s14, 0
	s_waitcnt lgkmcnt(6)
	v_mfma_f32_16x16x32_bf16 v[0:3], v[164:167], v[216:219], v[0:3]
	v_cvt_pk_bf16_f32 v242, v80, v81
	v_mfma_f32_16x16x32_bf16 v[4:7], v[164:167], v[238:241], v[4:7]
	v_exp_f32_e32 v89, v89
	ds_read_b128 v[160:163], v201 offset:4096
	s_waitcnt vmcnt(4)
	ds_write_b128 v225, v[136:139] offset:32768
	s_waitcnt lgkmcnt(7)
	v_mfma_f32_16x16x32_bf16 v[68:71], v[168:171], v[116:119], v[68:71]
	v_exp_f32_e32 v93, v93
	v_mfma_f32_16x16x32_bf16 v[64:67], v[168:171], v[100:103], v[64:67]
	v_cvt_pk_bf16_f32 v243, v82, v83
	ds_read_b128 v[164:167], v209 offset:57344
	s_waitcnt lgkmcnt(7)
	v_mfma_f32_16x16x32_bf16 v[12:15], v[172:175], v[238:241], v[12:15]
	v_exp_f32_e32 v90, v90
	v_mfma_f32_16x16x32_bf16 v[8:11], v[172:175], v[216:219], v[8:11]
	v_exp_f32_e32 v94, v94
	ds_read_b128 v[168:171], v202 offset:4096
	s_waitcnt lgkmcnt(7)
	v_mfma_f32_16x16x32_bf16 v[64:67], v[176:179], v[104:107], v[64:67]
	v_cvt_pk_bf16_f32 v204, v84, v85
	v_mfma_f32_16x16x32_bf16 v[68:71], v[176:179], v[120:123], v[68:71]
	v_exp_f32_e32 v91, v91
	ds_read_b128 v[172:175], v209 offset:59392
	ds_write_b128 v226, v[140:143] offset:32768
	s_waitcnt lgkmcnt(8)
	v_mfma_f32_16x16x32_bf16 v[16:19], v[180:183], v[216:219], v[16:19]
	v_exp_f32_e32 v95, v95
	v_mfma_f32_16x16x32_bf16 v[20:23], v[180:183], v[238:241], v[20:23]
	v_cvt_pk_bf16_f32 v205, v86, v87
	v_add_f32_e32 v220, v220, v88
	ds_read_b128 v[176:179], v203 offset:4096
	s_waitcnt lgkmcnt(8)
	v_mfma_f32_16x16x32_bf16 v[68:71], v[230:233], v[124:127], v[68:71]
	v_add_f32_e32 v221, v221, v92
	v_add_f32_e32 v220, v220, v89
	v_mfma_f32_16x16x32_bf16 v[64:67], v[230:233], v[108:111], v[64:67]
	v_add_f32_e32 v221, v221, v93
	v_cvt_pk_bf16_f32 v244, v88, v89
	ds_read_b128 v[180:183], v209 offset:61440
	s_waitcnt lgkmcnt(8)
	v_mfma_f32_16x16x32_bf16 v[28:31], v[234:237], v[238:241], v[28:31]
	v_cvt_pk_bf16_f32 v245, v90, v91
	v_cvt_pk_bf16_f32 v206, v92, v93
	v_mfma_f32_16x16x32_bf16 v[24:27], v[234:237], v[216:219], v[24:27]
	v_cvt_pk_bf16_f32 v207, v94, v95
	ds_read_b128 v[230:233], v246 offset:4096
	ds_write_b64 v227, v[148:149] offset:16384
	s_waitcnt lgkmcnt(9)
	v_mfma_f32_16x16x32_bf16 v[72:75], v[160:163], v[96:99], 0
	v_add_f32_e32 v220, v220, v90
	v_add_f32_e32 v221, v221, v94
	v_mfma_f32_16x16x32_bf16 v[76:79], v[160:163], v[112:115], 0
	v_add_f32_e32 v220, v220, v91
	v_add_f32_e32 v221, v221, v95
	ds_read_b128 v[234:237], v209 offset:63488
	s_waitcnt lgkmcnt(8)
	v_mfma_f32_16x16x32_bf16 v[32:35], v[164:167], v[216:219], v[32:35]
	v_add_f32_e32 v194, v194, v220
	v_add_f32_e32 v195, v195, v221
	v_mfma_f32_16x16x32_bf16 v[36:39], v[164:167], v[238:241], v[36:39]
	v_exp_f32_e32 v64, v64
	ds_read_b128 v[160:163], v201 offset:8192
	s_waitcnt lgkmcnt(8)
	v_mfma_f32_16x16x32_bf16 v[76:79], v[168:171], v[116:119], v[76:79]
	v_exp_f32_e32 v68, v68
	v_mfma_f32_16x16x32_bf16 v[72:75], v[168:171], v[100:103], v[72:75]
	v_exp_f32_e32 v65, v65
	ds_read_b128 v[164:167], v210 offset:49152
	ds_write_b64 v228, v[150:151] offset:16384
	s_waitcnt lgkmcnt(9)
	v_mfma_f32_16x16x32_bf16 v[44:47], v[172:175], v[238:241], v[44:47]
	v_exp_f32_e32 v69, v69
	v_mfma_f32_16x16x32_bf16 v[40:43], v[172:175], v[216:219], v[40:43]
	v_exp_f32_e32 v66, v66
	ds_read_b128 v[168:171], v202 offset:8192
	s_waitcnt lgkmcnt(8)
	v_mfma_f32_16x16x32_bf16 v[72:75], v[176:179], v[104:107], v[72:75]
	v_exp_f32_e32 v70, v70
	v_mfma_f32_16x16x32_bf16 v[76:79], v[176:179], v[120:123], v[76:79]
	v_exp_f32_e32 v67, v67
	ds_read_b128 v[172:175], v210 offset:51200
	s_waitcnt lgkmcnt(8)
	v_mfma_f32_16x16x32_bf16 v[48:51], v[180:183], v[216:219], v[48:51]
	v_exp_f32_e32 v71, v71
	v_mfma_f32_16x16x32_bf16 v[52:55], v[180:183], v[238:241], v[52:55]
	v_add_f32_e32 v220, v64, v65
	ds_read_b128 v[176:179], v203 offset:8192
	ds_write_b64 v229, v[144:145] offset:16384
	s_waitcnt lgkmcnt(9)
	v_mfma_f32_16x16x32_bf16 v[76:79], v[230:233], v[124:127], v[76:79]
	v_add_f32_e32 v221, v68, v69
	v_mfma_f32_16x16x32_bf16 v[72:75], v[230:233], v[108:111], v[72:75]
	v_add_f32_e32 v220, v220, v66
	ds_read_b128 v[180:183], v210 offset:53248
	s_waitcnt lgkmcnt(8)
	v_mfma_f32_16x16x32_bf16 v[60:63], v[234:237], v[238:241], v[60:63]
	v_add_f32_e32 v221, v221, v70
	v_add_f32_e32 v220, v220, v67
	v_mfma_f32_16x16x32_bf16 v[56:59], v[234:237], v[216:219], v[56:59]
	v_add_f32_e32 v221, v221, v71
	ds_read_b128 v[230:233], v246 offset:8192
	s_waitcnt lgkmcnt(8)
	v_mfma_f32_16x16x32_bf16 v[80:83], v[160:163], v[96:99], 0
	v_exp_f32_e32 v72, v72
	v_mfma_f32_16x16x32_bf16 v[84:87], v[160:163], v[112:115], 0
	v_exp_f32_e32 v76, v76
	ds_read_b128 v[234:237], v210 offset:55296
	ds_write_b64 v184, v[146:147] offset:16384
	s_waitcnt lgkmcnt(9)
	v_mfma_f32_16x16x32_bf16 v[0:3], v[164:167], v[242:245], v[0:3]
	v_exp_f32_e32 v73, v73
	v_mfma_f32_16x16x32_bf16 v[4:7], v[164:167], v[204:207], v[4:7]
	v_exp_f32_e32 v77, v77
	ds_read_b128 v[160:163], v201 offset:12288
	s_waitcnt lgkmcnt(8)
	v_mfma_f32_16x16x32_bf16 v[84:87], v[168:171], v[116:119], v[84:87]
	v_exp_f32_e32 v74, v74
	v_mfma_f32_16x16x32_bf16 v[80:83], v[168:171], v[100:103], v[80:83]
	v_exp_f32_e32 v78, v78
	ds_read_b128 v[164:167], v210 offset:57344
	s_waitcnt lgkmcnt(8)
	v_mfma_f32_16x16x32_bf16 v[12:15], v[172:175], v[204:207], v[12:15]
	v_exp_f32_e32 v75, v75
	v_mfma_f32_16x16x32_bf16 v[8:11], v[172:175], v[242:245], v[8:11]
	v_exp_f32_e32 v79, v79
	ds_read_b128 v[168:171], v202 offset:12288
	global_load_dwordx4 v[148:151], v198, s[8:9]
	s_waitcnt lgkmcnt(8)
	v_mfma_f32_16x16x32_bf16 v[80:83], v[176:179], v[104:107], v[80:83]
	v_add_f32_e32 v220, v220, v72
	v_add_f32_e32 v221, v221, v76
	v_mfma_f32_16x16x32_bf16 v[84:87], v[176:179], v[120:123], v[84:87]
	v_add_f32_e32 v220, v220, v73
	ds_read_b128 v[172:175], v210 offset:59392
	s_waitcnt lgkmcnt(7)
	v_mfma_f32_16x16x32_bf16 v[16:19], v[180:183], v[242:245], v[16:19]
	v_add_f32_e32 v221, v221, v77
	v_add_f32_e32 v220, v220, v74
	v_mfma_f32_16x16x32_bf16 v[20:23], v[180:183], v[204:207], v[20:23]
	v_add_f32_e32 v221, v221, v78
	ds_read_b128 v[176:179], v203 offset:12288
	s_waitcnt lgkmcnt(7)
	v_mfma_f32_16x16x32_bf16 v[84:87], v[230:233], v[124:127], v[84:87]
	v_add_f32_e32 v220, v220, v75
	v_add_f32_e32 v221, v221, v79
	v_mfma_f32_16x16x32_bf16 v[80:83], v[230:233], v[108:111], v[80:83]
	v_cvt_pk_bf16_f32 v216, v64, v65
	ds_read_b128 v[180:183], v210 offset:61440
	global_load_dwordx4 v[144:147], v199, s[8:9]
	s_waitcnt lgkmcnt(7)
	v_mfma_f32_16x16x32_bf16 v[28:31], v[234:237], v[204:207], v[28:31]
	v_cvt_pk_bf16_f32 v217, v66, v67
	v_cvt_pk_bf16_f32 v238, v68, v69
	v_mfma_f32_16x16x32_bf16 v[24:27], v[234:237], v[242:245], v[24:27]
	v_cvt_pk_bf16_f32 v239, v70, v71
	ds_read_b128 v[230:233], v246 offset:12288
	s_waitcnt lgkmcnt(6)
	v_mfma_f32_16x16x32_bf16 v[88:91], v[160:163], v[96:99], 0
	v_exp_f32_e32 v80, v80
	v_mfma_f32_16x16x32_bf16 v[92:95], v[160:163], v[112:115], 0
	v_exp_f32_e32 v84, v84
	ds_read_b128 v[234:237], v210 offset:63488
	s_waitcnt lgkmcnt(6)
	v_mfma_f32_16x16x32_bf16 v[32:35], v[164:167], v[242:245], v[32:35]
	v_exp_f32_e32 v81, v81
	v_mfma_f32_16x16x32_bf16 v[36:39], v[164:167], v[204:207], v[36:39]
	v_exp_f32_e32 v85, v85
	global_load_dwordx4 v[136:139], v196, s[6:7]
	s_waitcnt lgkmcnt(5)
	v_mfma_f32_16x16x32_bf16 v[92:95], v[168:171], v[116:119], v[92:95]
	v_exp_f32_e32 v82, v82
	v_mfma_f32_16x16x32_bf16 v[88:91], v[168:171], v[100:103], v[88:91]
	v_exp_f32_e32 v86, v86
	s_waitcnt lgkmcnt(4)
	v_mfma_f32_16x16x32_bf16 v[44:47], v[172:175], v[204:207], v[44:47]
	v_exp_f32_e32 v83, v83
	v_mfma_f32_16x16x32_bf16 v[40:43], v[172:175], v[242:245], v[40:43]
	v_exp_f32_e32 v87, v87
	s_waitcnt lgkmcnt(3)
	v_mfma_f32_16x16x32_bf16 v[88:91], v[176:179], v[104:107], v[88:91]
	v_add_f32_e32 v220, v220, v80
	v_add_f32_e32 v221, v221, v84
	v_mfma_f32_16x16x32_bf16 v[92:95], v[176:179], v[120:123], v[92:95]
	v_add_f32_e32 v220, v220, v81
	global_load_dwordx4 v[140:143], v197, s[6:7]
	s_waitcnt lgkmcnt(2)
	v_mfma_f32_16x16x32_bf16 v[48:51], v[180:183], v[242:245], v[48:51]
	v_add_f32_e32 v221, v221, v85
	v_add_f32_e32 v220, v220, v82
	v_mfma_f32_16x16x32_bf16 v[52:55], v[180:183], v[204:207], v[52:55]
	v_add_f32_e32 v221, v221, v86
	s_waitcnt lgkmcnt(1)
	v_mfma_f32_16x16x32_bf16 v[92:95], v[230:233], v[124:127], v[92:95]
	v_add_f32_e32 v220, v220, v83
	v_add_f32_e32 v221, v221, v87
	v_mfma_f32_16x16x32_bf16 v[88:91], v[230:233], v[108:111], v[88:91]
	v_cvt_pk_bf16_f32 v218, v72, v73
	s_add_u32 s10, s10, 0x200
	s_addc_u32 s11, s11, 0
	s_add_u32 s12, s12, 0x40000
	s_addc_u32 s13, s13, 0
	s_add_i32 s4, s4, 4
	s_cmpk_lt_u32 s4, 0x104
	s_cselect_b64 s[6:7], -1, 0
	s_and_b64 s[6:7], s[0:1], s[6:7]
	s_and_b64 vcc, exec, s[6:7]
	s_waitcnt lgkmcnt(0)
	v_mfma_f32_16x16x32_bf16 v[60:63], v[234:237], v[204:207], v[60:63]
	v_cvt_pk_bf16_f32 v219, v74, v75
	v_cvt_pk_bf16_f32 v240, v76, v77
	v_mfma_f32_16x16x32_bf16 v[56:59], v[234:237], v[242:245], v[56:59]
	v_cvt_pk_bf16_f32 v241, v78, v79
	s_cbranch_vccnz .LBB0_734
	s_waitcnt vmcnt(0)
	s_nop 7
	s_nop 7
	ds_swizzle_b32 v64, v194 offset:swizzle(SWAP,16)
	s_waitcnt lgkmcnt(0)
	v_add_f32_e32 v194, v194, v64
	v_mov_b32_e32 v65, v194
	s_nop 1
	v_permlane32_swap_b32_e32 v194, v65
	v_add_f32_e32 v194, v194, v65
	s_nop 0
	v_rcp_f32_e32 v66, v194
	ds_swizzle_b32 v64, v195 offset:swizzle(SWAP,16)
	s_waitcnt lgkmcnt(0)
	v_add_f32_e32 v195, v195, v64
	v_mov_b32_e32 v65, v195
	s_nop 1
	v_permlane32_swap_b32_e32 v195, v65
	v_add_f32_e32 v195, v195, v65
	s_nop 0
	v_rcp_f32_e32 v67, v195
	v_readlane_b32 s100, v250, 8
	v_mbcnt_lo_u32_b32 v68, -1, 0
	v_mbcnt_hi_u32_b32 v68, -1, v68
	v_and_b32_e32 v69, 15, v68
	v_lshrrev_b32_e32 v70, 4, v68
	s_lshr_b32 s101, s100, 1
	v_add_u32_e32 v69, s101, v69
	v_lshlrev_b32_e32 v69, 12, v69
	v_and_b32_e32 v71, 1, v70
	v_lshlrev_b32_e32 v71, 5, v71
	v_and_b32_e32 v70, 2, v70
	v_lshl_add_u32 v71, v70, 3, v71
	v_add_u32_e32 v70, v69, v71
	v_add_u32_e32 v71, 0x10000, v70
	v_mul_f32_e32 v0, v0, v66
	v_mul_f32_e32 v1, v1, v66
	v_mul_f32_e32 v2, v2, v66
	v_mul_f32_e32 v3, v3, v66
	v_mul_f32_e32 v8, v8, v66
	v_mul_f32_e32 v9, v9, v66
	v_mul_f32_e32 v10, v10, v66
	v_mul_f32_e32 v11, v11, v66
	v_cvt_pk_bf16_f32 v72, v0, v1
	v_cvt_pk_bf16_f32 v73, v2, v3
	v_cvt_pk_bf16_f32 v74, v8, v9
	v_cvt_pk_bf16_f32 v75, v10, v11
	s_nop 1
	v_permlane16_swap_b32_e32 v72, v74
	v_permlane16_swap_b32_e32 v73, v75
	s_nop 1
	global_store_dwordx4 v70, v[72:75], s[58:59] offset:0
	v_mul_f32_e32 v16, v16, v66
	v_mul_f32_e32 v17, v17, v66
	v_mul_f32_e32 v18, v18, v66
	v_mul_f32_e32 v19, v19, v66
	v_mul_f32_e32 v24, v24, v66
	v_mul_f32_e32 v25, v25, v66
	v_mul_f32_e32 v26, v26, v66
	v_mul_f32_e32 v27, v27, v66
	v_cvt_pk_bf16_f32 v76, v16, v17
	v_cvt_pk_bf16_f32 v77, v18, v19
	v_cvt_pk_bf16_f32 v78, v24, v25
	v_cvt_pk_bf16_f32 v79, v26, v27
	s_nop 1
	v_permlane16_swap_b32_e32 v76, v78
	v_permlane16_swap_b32_e32 v77, v79
	s_nop 1
	global_store_dwordx4 v70, v[76:79], s[58:59] offset:64
	v_mul_f32_e32 v32, v32, v66
	v_mul_f32_e32 v33, v33, v66
	v_mul_f32_e32 v34, v34, v66
	v_mul_f32_e32 v35, v35, v66
	v_mul_f32_e32 v40, v40, v66
	v_mul_f32_e32 v41, v41, v66
	v_mul_f32_e32 v42, v42, v66
	v_mul_f32_e32 v43, v43, v66
	v_cvt_pk_bf16_f32 v80, v32, v33
	v_cvt_pk_bf16_f32 v81, v34, v35
	v_cvt_pk_bf16_f32 v82, v40, v41
	v_cvt_pk_bf16_f32 v83, v42, v43
	s_nop 1
	v_permlane16_swap_b32_e32 v80, v82
	v_permlane16_swap_b32_e32 v81, v83
	s_nop 1
	global_store_dwordx4 v70, v[80:83], s[58:59] offset:128
	v_mul_f32_e32 v48, v48, v66
	v_mul_f32_e32 v49, v49, v66
	v_mul_f32_e32 v50, v50, v66
	v_mul_f32_e32 v51, v51, v66
	v_mul_f32_e32 v56, v56, v66
	v_mul_f32_e32 v57, v57, v66
	v_mul_f32_e32 v58, v58, v66
	v_mul_f32_e32 v59, v59, v66
	v_cvt_pk_bf16_f32 v84, v48, v49
	v_cvt_pk_bf16_f32 v85, v50, v51
	v_cvt_pk_bf16_f32 v86, v56, v57
	v_cvt_pk_bf16_f32 v87, v58, v59
	s_nop 1
	v_permlane16_swap_b32_e32 v84, v86
	v_permlane16_swap_b32_e32 v85, v87
	s_nop 1
	global_store_dwordx4 v70, v[84:87], s[58:59] offset:192
	v_mul_f32_e32 v4, v4, v67
	v_mul_f32_e32 v5, v5, v67
	v_mul_f32_e32 v6, v6, v67
	v_mul_f32_e32 v7, v7, v67
	v_mul_f32_e32 v12, v12, v67
	v_mul_f32_e32 v13, v13, v67
	v_mul_f32_e32 v14, v14, v67
	v_mul_f32_e32 v15, v15, v67
	v_cvt_pk_bf16_f32 v88, v4, v5
	v_cvt_pk_bf16_f32 v89, v6, v7
	v_cvt_pk_bf16_f32 v90, v12, v13
	v_cvt_pk_bf16_f32 v91, v14, v15
	s_nop 1
	v_permlane16_swap_b32_e32 v88, v90
	v_permlane16_swap_b32_e32 v89, v91
	s_nop 1
	global_store_dwordx4 v71, v[88:91], s[58:59] offset:0
	v_mul_f32_e32 v20, v20, v67
	v_mul_f32_e32 v21, v21, v67
	v_mul_f32_e32 v22, v22, v67
	v_mul_f32_e32 v23, v23, v67
	v_mul_f32_e32 v28, v28, v67
	v_mul_f32_e32 v29, v29, v67
	v_mul_f32_e32 v30, v30, v67
	v_mul_f32_e32 v31, v31, v67
	v_cvt_pk_bf16_f32 v92, v20, v21
	v_cvt_pk_bf16_f32 v93, v22, v23
	v_cvt_pk_bf16_f32 v94, v28, v29
	v_cvt_pk_bf16_f32 v95, v30, v31
	s_nop 1
	v_permlane16_swap_b32_e32 v92, v94
	v_permlane16_swap_b32_e32 v93, v95
	s_nop 1
	global_store_dwordx4 v71, v[92:95], s[58:59] offset:64
	v_mul_f32_e32 v36, v36, v67
	v_mul_f32_e32 v37, v37, v67
	v_mul_f32_e32 v38, v38, v67
	v_mul_f32_e32 v39, v39, v67
	v_mul_f32_e32 v44, v44, v67
	v_mul_f32_e32 v45, v45, v67
	v_mul_f32_e32 v46, v46, v67
	v_mul_f32_e32 v47, v47, v67
	v_cvt_pk_bf16_f32 v72, v36, v37
	v_cvt_pk_bf16_f32 v73, v38, v39
	v_cvt_pk_bf16_f32 v74, v44, v45
	v_cvt_pk_bf16_f32 v75, v46, v47
	s_nop 1
	v_permlane16_swap_b32_e32 v72, v74
	v_permlane16_swap_b32_e32 v73, v75
	s_nop 1
	global_store_dwordx4 v71, v[72:75], s[58:59] offset:128
	v_mul_f32_e32 v52, v52, v67
	v_mul_f32_e32 v53, v53, v67
	v_mul_f32_e32 v54, v54, v67
	v_mul_f32_e32 v55, v55, v67
	v_mul_f32_e32 v60, v60, v67
	v_mul_f32_e32 v61, v61, v67
	v_mul_f32_e32 v62, v62, v67
	v_mul_f32_e32 v63, v63, v67
	v_cvt_pk_bf16_f32 v76, v52, v53
	v_cvt_pk_bf16_f32 v77, v54, v55
	v_cvt_pk_bf16_f32 v78, v60, v61
	v_cvt_pk_bf16_f32 v79, v62, v63
	s_nop 1
	v_permlane16_swap_b32_e32 v76, v78
	v_permlane16_swap_b32_e32 v77, v79
	s_nop 1
	global_store_dwordx4 v71, v[76:79], s[58:59] offset:192
	s_barrier
